# combo7 + attention: Q tile prefetched one tile ahead, K and V fragment LDS reads issued ahead of their MFMAs, unit staging loads batched
# speedup vs baseline: 1.0295x; 1.0295x over previous
.LBB0_549:
	s_lshl_b32 s8, s14, 7
	s_ashr_i32 s4, s14, 6
	s_bfe_u32 s5, s14, 0x20004
	s_and_b32 s21, s8, 0x780
	s_add_i32 s12, s21, 0xffffff80
	s_lshl_b32 s13, s4, 11
	s_lshl_b32 s8, s5, 7
	s_cmp_eq_u32 s21, 0
	v_lshl_add_u64 v[6:7], v[44:45], 0, s[8:9]
	s_barrier
	v_mov_b64_e32 v[114:115], 0
	v_mov_b64_e32 v[116:117], 0
	v_mov_b64_e32 v[118:119], 0
	v_mov_b64_e32 v[120:121], 0
	v_mov_b64_e32 v[122:123], 0
	v_mov_b64_e32 v[124:125], 0
	v_mov_b64_e32 v[126:127], 0
	v_mov_b64_e32 v[128:129], 0
	v_mov_b64_e32 v[130:131], 0
	v_mov_b64_e32 v[132:133], 0
	v_mov_b64_e32 v[134:135], 0
	v_mov_b64_e32 v[136:137], 0
	v_mov_b64_e32 v[138:139], 0
	v_mov_b64_e32 v[140:141], 0
	v_mov_b64_e32 v[142:143], 0
	v_mov_b64_e32 v[144:145], 0
	s_add_i32 s8, s12, s13
	s_cmp_eq_u32 s21, 0
	s_cbranch_scc1 .Lattn_k23
	v_or_b32_e32 v2, s8, v69
	v_ashrrev_i32_e32 v3, 31, v2
	v_lshlrev_b64 v[2:3], 9, v[2:3]
	v_lshl_add_u64 v[2:3], v[6:7], 0, v[2:3]
	global_load_dwordx4 v[114:117], v[2:3], off
	v_add_u32_e32 v2, s8, v70
	v_ashrrev_i32_e32 v3, 31, v2
	v_lshlrev_b64 v[2:3], 9, v[2:3]
	v_lshl_add_u64 v[2:3], v[6:7], 0, v[2:3]
	global_load_dwordx4 v[118:121], v[2:3], off
.Lattn_k23:
	v_add_u32_e32 v8, s8, v71
	v_ashrrev_i32_e32 v9, 31, v8
	v_lshlrev_b64 v[8:9], 9, v[8:9]
	v_lshl_add_u64 v[14:15], v[6:7], 0, v[8:9]
	v_add_u32_e32 v8, s8, v72
	v_ashrrev_i32_e32 v9, 31, v8
	v_lshlrev_b64 v[8:9], 9, v[8:9]
	v_lshl_add_u64 v[16:17], v[6:7], 0, v[8:9]
	global_load_dwordx4 v[122:125], v[14:15], off
	global_load_dwordx4 v[126:129], v[16:17], off
	v_add_u32_e32 v42, s12, v49
	v_cmp_le_i32_e32 vcc, 0, v42
	s_and_saveexec_b64 s[10:11], vcc
	s_lshl_b32 s8, s4, 2
	s_or_b32 s12, s8, s5
	s_ashr_i32 s13, s12, 31
	s_lshl_b64 s[12:13], s[12:13], 18
	s_add_u32 s12, s15, s12
	s_addc_u32 s13, s16, s13
	v_lshl_add_u64 v[2:3], v[42:43], 1, s[12:13]
	v_mov_b32_e32 v53, v43
	v_mov_b32_e32 v55, v43
	v_mov_b32_e32 v57, v43
	v_mov_b32_e32 v59, v43
	v_lshl_add_u64 v[4:5], v[2:3], 0, v[52:53]
	v_lshl_add_u64 v[6:7], v[2:3], 0, v[54:55]
	v_lshl_add_u64 v[18:19], v[2:3], 0, v[56:57]
	v_lshl_add_u64 v[20:21], v[2:3], 0, v[58:59]
	global_load_dwordx4 v[130:133], v[4:5], off
	global_load_dwordx4 v[134:137], v[6:7], off
	global_load_dwordx4 v[138:141], v[18:19], off
	global_load_dwordx4 v[142:145], v[20:21], off
	s_mov_b64 exec, s[10:11]
	s_waitcnt vmcnt(0)
	ds_write_b128 v76, v[114:117]
	ds_write_b128 v77, v[118:121]
	ds_write_b128 v78, v[122:125]
	ds_write_b128 v79, v[126:129]
	ds_write_b128 v83, v[130:133] offset:36864
	ds_write_b128 v84, v[134:137] offset:36864
	ds_write_b128 v81, v[138:141] offset:36864
	ds_write_b128 v82, v[142:145] offset:36864
	v_lshlrev_b32_e32 v2, 2, v64
	v_lshl_or_b32 v2, s5, 4, v2
	s_waitcnt lgkmcnt(0)
	s_barrier
	global_load_dword v53, v2, s[6:7]
	v_mov_b32_e32 v252, v2
	s_lshr_b32 s5, s14, 4
	s_and_b32 s5, s5, 3
	s_lshl_b32 s10, s5, 9
	s_ashr_i32 s5, s4, 31
	s_and_b32 s8, s18, 0x780
	s_lshl_b64 s[4:5], s[4:5], 11
	v_or_b32_e32 v42, s8, v1
	v_mov_b32_e32 v3, s5
	v_or_b32_e32 v2, s4, v48
	v_lshl_add_u64 v[2:3], v[2:3], 0, v[42:43]
	v_lshlrev_b64 v[2:3], 11, v[2:3]
	v_or3_b32 v2, s10, v80, v2
	s_sub_i32 s8, 0x7f, s21
	v_lshl_add_u64 v[60:61], v[46:47], 0, v[2:3]
	v_lshl_add_u64 v[62:63], v[50:51], 0, v[2:3]
	s_mov_b64 s[10:11], 0
	v_mov_b32_e32 v42, v75
	v_mov_b32_e32 v55, v74
	v_lshl_add_u64 v[250:251], v[60:61], 0, s[10:11]
	v_add_co_u32_e32 v250, vcc, 0x3bc4a000, v250
	s_nop 1
	v_addc_co_u32_e32 v251, vcc, 0, v251, vcc
	global_load_dwordx4 v[242:245], v[250:251], off
	global_load_dwordx4 v[246:249], v[250:251], off offset:64
	global_load_dword v53, v252, s[6:7]
	global_load_dword v53, v252, s[6:7]
	global_load_dword v53, v252, s[6:7]
	global_load_dword v53, v252, s[6:7]
.LBB0_559:
	v_lshl_add_u64 v[2:3], v[60:61], 0, s[10:11]
	v_add_co_u32_e32 v6, vcc, 0x3bc4a000, v2
	v_min_u32_e32 v88, 6, v42
	s_nop 0
	v_addc_co_u32_e32 v7, vcc, 0, v3, vcc
	s_waitcnt vmcnt(4)
	v_mov_b32_e32 v2, v242
	v_mov_b32_e32 v3, v243
	v_mov_b32_e32 v4, v244
	v_mov_b32_e32 v5, v245
	v_mov_b32_e32 v90, v246
	v_mov_b32_e32 v91, v247
	v_mov_b32_e32 v92, v248
	v_mov_b32_e32 v93, v249
	v_add_co_u32_e32 v250, vcc, 0x8000, v6
	s_nop 1
	v_addc_co_u32_e32 v251, vcc, 0, v7, vcc
	global_load_dwordx4 v[242:245], v[250:251], off
	global_load_dwordx4 v[246:249], v[250:251], off offset:64
	v_lshlrev_b32_e32 v89, 4, v88
	v_add_u32_e32 v98, 16, v89
	v_add_u32_e32 v87, 2, v88
	v_lshlrev_b32_e32 v99, 4, v87
	v_add_u32_e32 v100, 48, v89
	v_add_u32_e32 v86, 4, v88
	v_lshlrev_b32_e32 v101, 4, v86
	v_add_u32_e32 v102, 0x50, v89
	v_add_u32_e32 v59, 6, v88
	v_lshlrev_b32_e32 v103, 4, v59
	v_add_u32_e32 v104, 0x70, v89
	v_or_b32_e32 v57, 8, v88
	v_lshlrev_b32_e32 v105, 4, v57
	v_add_u32_e32 v106, 0x90, v89
	v_or_b32_e32 v252, v89, v1
	v_mad_u32_u24 v253, v252, s17, v65
	ds_read_b128 v[114:117], v253
	ds_read_b128 v[118:121], v253 offset:64
	v_or_b32_e32 v252, v98, v1
	v_mad_u32_u24 v253, v252, s17, v65
	ds_read_b128 v[122:125], v253
	ds_read_b128 v[126:129], v253 offset:64
	v_or_b32_e32 v252, v99, v1
	v_mad_u32_u24 v253, v252, s17, v65
	ds_read_b128 v[130:133], v253
	ds_read_b128 v[134:137], v253 offset:64
	v_or_b32_e32 v252, v100, v1
	v_mad_u32_u24 v253, v252, s17, v65
	ds_read_b128 v[138:141], v253
	ds_read_b128 v[142:145], v253 offset:64
	v_or_b32_e32 v252, v101, v1
	v_mad_u32_u24 v253, v252, s17, v65
	ds_read_b128 v[146:149], v253
	ds_read_b128 v[150:153], v253 offset:64
	v_or_b32_e32 v252, v102, v1
	v_mad_u32_u24 v253, v252, s17, v65
	ds_read_b128 v[154:157], v253
	ds_read_b128 v[158:161], v253 offset:64
	v_or_b32_e32 v252, v103, v1
	v_mad_u32_u24 v253, v252, s17, v65
	ds_read_b128 v[162:165], v253
	ds_read_b128 v[166:169], v253 offset:64
	v_or_b32_e32 v252, v104, v1
	v_mad_u32_u24 v253, v252, s17, v65
	ds_read_b128 v[170:173], v253
	ds_read_b128 v[174:177], v253 offset:64
	v_or_b32_e32 v252, v105, v1
	v_mad_u32_u24 v253, v252, s17, v65
	ds_read_b128 v[178:181], v253
	ds_read_b128 v[182:185], v253 offset:64
	v_or_b32_e32 v252, v106, v1
	v_mad_u32_u24 v253, v252, s17, v65
	ds_read_b128 v[186:189], v253
	ds_read_b128 v[190:193], v253 offset:64
	v_or_b32_e32 v89, v89, v66
	v_cmp_gt_u32_e32 vcc, v89, v55
	v_cmp_lt_i32_e64 s[4:5], s8, v89
	s_and_b64 vcc, vcc, s[4:5]
	v_cmp_le_i32_e64 s[4:5], s8, v89
	v_add_u32_e32 v42, 1, v42
	s_waitcnt lgkmcnt(15)
	v_mfma_f32_16x16x32_bf16 v[38:41], v[114:117], v[2:5], 0
	v_mfma_f32_16x16x32_bf16 v[38:41], v[118:121], v[90:93], v[38:41]
	s_waitcnt lgkmcnt(15)
	v_mfma_f32_16x16x32_bf16 v[34:37], v[122:125], v[2:5], 0
	v_mfma_f32_16x16x32_bf16 v[34:37], v[126:129], v[90:93], v[34:37]
	s_waitcnt lgkmcnt(14)
	v_mfma_f32_16x16x32_bf16 v[30:33], v[130:133], v[2:5], 0
	v_mfma_f32_16x16x32_bf16 v[30:33], v[134:137], v[90:93], v[30:33]
	s_waitcnt lgkmcnt(12)
	v_mfma_f32_16x16x32_bf16 v[26:29], v[138:141], v[2:5], 0
	v_mfma_f32_16x16x32_bf16 v[26:29], v[142:145], v[90:93], v[26:29]
	s_waitcnt lgkmcnt(10)
	v_mfma_f32_16x16x32_bf16 v[22:25], v[146:149], v[2:5], 0
	v_mfma_f32_16x16x32_bf16 v[22:25], v[150:153], v[90:93], v[22:25]
	s_waitcnt lgkmcnt(8)
	v_mfma_f32_16x16x32_bf16 v[18:21], v[154:157], v[2:5], 0
	v_mfma_f32_16x16x32_bf16 v[18:21], v[158:161], v[90:93], v[18:21]
	s_waitcnt lgkmcnt(6)
	v_mfma_f32_16x16x32_bf16 v[14:17], v[162:165], v[2:5], 0
	v_mfma_f32_16x16x32_bf16 v[14:17], v[166:169], v[90:93], v[14:17]
	s_waitcnt lgkmcnt(4)
	v_mfma_f32_16x16x32_bf16 v[10:13], v[170:173], v[2:5], 0
	v_mfma_f32_16x16x32_bf16 v[10:13], v[174:177], v[90:93], v[10:13]
	s_waitcnt lgkmcnt(2)
	v_mfma_f32_16x16x32_bf16 v[6:9], v[178:181], v[2:5], 0
	v_mfma_f32_16x16x32_bf16 v[6:9], v[182:185], v[90:93], v[6:9]
	s_waitcnt lgkmcnt(0)
	v_mfma_f32_16x16x32_bf16 v[2:5], v[186:189], v[2:5], 0
	v_mfma_f32_16x16x32_bf16 v[2:5], v[190:193], v[90:93], v[2:5]
	v_lshl_add_u32 v252, v88, 5, v73
	v_add_u32_e32 v253, 0x9000, v252
	ds_read2_b64 v[194:197], v253 offset1:4
	v_add_u32_e32 v253, 0xb000, v252
	ds_read2_b64 v[198:201], v253 offset0:32 offset1:36
	v_add_u32_e32 v253, 0xd000, v252
	ds_read2_b64 v[202:205], v253 offset0:64 offset1:68
	v_add_u32_e32 v253, 0xf000, v252
	ds_read2_b64 v[206:209], v253 offset0:96 offset1:100
	v_lshl_add_u32 v252, v87, 5, v73
	v_add_u32_e32 v253, 0x9000, v252
	ds_read2_b64 v[210:213], v253 offset1:4
	v_add_u32_e32 v253, 0xb000, v252
	ds_read2_b64 v[214:217], v253 offset0:32 offset1:36
	v_add_u32_e32 v253, 0xd000, v252
	ds_read2_b64 v[218:221], v253 offset0:64 offset1:68
	v_add_u32_e32 v253, 0xf000, v252
	ds_read2_b64 v[222:225], v253 offset0:96 offset1:100
	v_lshl_add_u32 v252, v86, 5, v73
	v_add_u32_e32 v253, 0x9000, v252
	ds_read2_b64 v[226:229], v253 offset1:4
	v_add_u32_e32 v253, 0xb000, v252
	ds_read2_b64 v[230:233], v253 offset0:32 offset1:36
	v_add_u32_e32 v253, 0xd000, v252
	ds_read2_b64 v[234:237], v253 offset0:64 offset1:68
	v_add_u32_e32 v253, 0xf000, v252
	ds_read2_b64 v[238:241], v253 offset0:96 offset1:100
	v_lshl_add_u32 v252, v59, 5, v73
	v_add_u32_e32 v253, 0x9000, v252
	ds_read2_b64 v[114:117], v253 offset1:4
	v_add_u32_e32 v253, 0xb000, v252
	ds_read2_b64 v[118:121], v253 offset0:32 offset1:36
	v_add_u32_e32 v253, 0xd000, v252
	ds_read2_b64 v[122:125], v253 offset0:64 offset1:68
	v_add_u32_e32 v253, 0xf000, v252
	ds_read2_b64 v[126:129], v253 offset0:96 offset1:100
	v_lshl_add_u32 v252, v57, 5, v73
	v_add_u32_e32 v253, 0x9000, v252
	ds_read2_b64 v[130:133], v253 offset1:4
	v_add_u32_e32 v253, 0xb000, v252
	ds_read2_b64 v[134:137], v253 offset0:32 offset1:36
	v_add_u32_e32 v253, 0xd000, v252
	ds_read2_b64 v[138:141], v253 offset0:64 offset1:68
	v_add_u32_e32 v253, 0xf000, v252
	ds_read2_b64 v[142:145], v253 offset0:96 offset1:100
	v_cndmask_b32_e32 v38, v85, v38, vcc
	v_cmp_ge_u32_e32 vcc, v89, v55
	s_and_b64 vcc, vcc, s[4:5]
	s_nop 1
	v_cndmask_b32_e32 v39, v85, v39, vcc
	v_or_b32_e32 v92, 2, v89
	v_cmp_gt_u32_e32 vcc, v92, v55
	v_cmp_lt_i32_e64 s[4:5], s8, v92
	s_and_b64 vcc, vcc, s[4:5]
	v_or_b32_e32 v89, 3, v89
	v_cndmask_b32_e32 v40, v85, v40, vcc
	v_cmp_gt_u32_e32 vcc, v89, v55
	v_cmp_lt_i32_e64 s[4:5], s8, v89
	s_and_b64 vcc, vcc, s[4:5]
	v_max3_f32 v91, v38, s20, v39
	v_cndmask_b32_e32 v41, v85, v41, vcc
	v_max3_f32 v89, v91, v40, v41
	v_or_b32_e32 v91, v98, v66
	v_cmp_gt_u32_e32 vcc, v91, v55
	v_cmp_lt_i32_e64 s[4:5], s8, v91
	s_and_b64 vcc, vcc, s[4:5]
	v_cndmask_b32_e32 v34, v85, v34, vcc
	v_cmp_ge_u32_e32 vcc, v91, v55
	v_cmp_le_i32_e64 s[4:5], s8, v91
	s_and_b64 vcc, vcc, s[4:5]
	v_or_b32_e32 v92, 2, v91
	v_cndmask_b32_e32 v35, v85, v35, vcc
	v_cmp_gt_u32_e32 vcc, v92, v55
	v_cmp_lt_i32_e64 s[4:5], s8, v92
	s_and_b64 vcc, vcc, s[4:5]
	v_or_b32_e32 v91, 3, v91
	v_cndmask_b32_e32 v36, v85, v36, vcc
	v_cmp_gt_u32_e32 vcc, v91, v55
	v_cmp_lt_i32_e64 s[4:5], s8, v91
	s_and_b64 vcc, vcc, s[4:5]
	v_or_b32_e32 v91, v99, v66
	v_cndmask_b32_e32 v37, v85, v37, vcc
	v_cmp_gt_u32_e32 vcc, v91, v55
	v_cmp_lt_i32_e64 s[4:5], s8, v91
	s_and_b64 vcc, vcc, s[4:5]
	v_cndmask_b32_e32 v30, v85, v30, vcc
	v_cmp_ge_u32_e32 vcc, v91, v55
	v_cmp_le_i32_e64 s[4:5], s8, v91
	s_and_b64 vcc, vcc, s[4:5]
	v_or_b32_e32 v92, 2, v91
	v_cndmask_b32_e32 v31, v85, v31, vcc
	v_cmp_gt_u32_e32 vcc, v92, v55
	v_cmp_lt_i32_e64 s[4:5], s8, v92
	s_and_b64 vcc, vcc, s[4:5]
	v_or_b32_e32 v91, 3, v91
	v_cndmask_b32_e32 v32, v85, v32, vcc
	v_cmp_gt_u32_e32 vcc, v91, v55
	v_cmp_lt_i32_e64 s[4:5], s8, v91
	v_add_u32_e32 v90, 0x80, v55
	s_and_b64 vcc, vcc, s[4:5]
	v_or_b32_e32 v91, v100, v66
	v_cndmask_b32_e32 v33, v85, v33, vcc
	v_cmp_gt_u32_e32 vcc, v91, v55
	v_cmp_le_u32_e64 s[4:5], v91, v90
	s_and_b64 s[4:5], vcc, s[4:5]
	v_cmp_lt_i32_e32 vcc, s8, v91
	s_and_b64 vcc, s[4:5], vcc
	v_cmp_lt_u32_e64 s[4:5], v91, v90
	v_cndmask_b32_e32 v26, v85, v26, vcc
	v_cmp_ge_u32_e32 vcc, v91, v55
	s_and_b64 s[4:5], vcc, s[4:5]
	v_cmp_le_i32_e32 vcc, s8, v91
	s_and_b64 vcc, s[4:5], vcc
	v_or_b32_e32 v92, 2, v91
	v_cndmask_b32_e32 v27, v85, v27, vcc
	v_cmp_gt_u32_e32 vcc, v92, v55
	v_cmp_le_u32_e64 s[4:5], v92, v90
	s_and_b64 s[4:5], vcc, s[4:5]
	v_cmp_lt_i32_e32 vcc, s8, v92
	s_and_b64 vcc, s[4:5], vcc
	v_or_b32_e32 v91, 3, v91
	v_cndmask_b32_e32 v28, v85, v28, vcc
	v_cmp_gt_u32_e32 vcc, v91, v55
	v_cmp_le_u32_e64 s[4:5], v91, v90
	s_and_b64 s[4:5], vcc, s[4:5]
	v_cmp_lt_i32_e32 vcc, s8, v91
	s_and_b64 vcc, s[4:5], vcc
	v_or_b32_e32 v91, v101, v66
	v_cndmask_b32_e32 v29, v85, v29, vcc
	v_cmp_gt_u32_e32 vcc, v91, v55
	v_cmp_le_u32_e64 s[4:5], v91, v90
	s_and_b64 s[4:5], vcc, s[4:5]
	v_cmp_lt_i32_e32 vcc, s8, v91
	s_and_b64 vcc, s[4:5], vcc
	v_cmp_lt_u32_e64 s[4:5], v91, v90
	v_cndmask_b32_e32 v22, v85, v22, vcc
	v_cmp_ge_u32_e32 vcc, v91, v55
	s_and_b64 s[4:5], vcc, s[4:5]
	v_cmp_le_i32_e32 vcc, s8, v91
	s_and_b64 vcc, s[4:5], vcc
	v_or_b32_e32 v92, 2, v91
	v_cndmask_b32_e32 v23, v85, v23, vcc
	v_cmp_gt_u32_e32 vcc, v92, v55
	v_cmp_le_u32_e64 s[4:5], v92, v90
	s_and_b64 s[4:5], vcc, s[4:5]
	v_cmp_lt_i32_e32 vcc, s8, v92
	s_and_b64 vcc, s[4:5], vcc
	v_or_b32_e32 v91, 3, v91
	v_cndmask_b32_e32 v24, v85, v24, vcc
	v_cmp_gt_u32_e32 vcc, v91, v55
	v_cmp_le_u32_e64 s[4:5], v91, v90
	s_and_b64 s[4:5], vcc, s[4:5]
	v_cmp_lt_i32_e32 vcc, s8, v91
	s_and_b64 vcc, s[4:5], vcc
	v_or_b32_e32 v91, v102, v66
	v_cndmask_b32_e32 v25, v85, v25, vcc
	v_cmp_gt_u32_e32 vcc, v91, v55
	v_cmp_le_u32_e64 s[4:5], v91, v90
	s_and_b64 s[4:5], vcc, s[4:5]
	v_cmp_lt_i32_e32 vcc, s8, v91
	s_and_b64 vcc, s[4:5], vcc
	v_cmp_lt_u32_e64 s[4:5], v91, v90
	v_cndmask_b32_e32 v18, v85, v18, vcc
	v_cmp_ge_u32_e32 vcc, v91, v55
	s_and_b64 s[4:5], vcc, s[4:5]
	v_cmp_le_i32_e32 vcc, s8, v91
	s_and_b64 vcc, s[4:5], vcc
	v_or_b32_e32 v92, 2, v91
	v_cndmask_b32_e32 v19, v85, v19, vcc
	v_cmp_gt_u32_e32 vcc, v92, v55
	v_cmp_le_u32_e64 s[4:5], v92, v90
	s_and_b64 s[4:5], vcc, s[4:5]
	v_cmp_lt_i32_e32 vcc, s8, v92
	s_and_b64 vcc, s[4:5], vcc
	v_or_b32_e32 v91, 3, v91
	v_cndmask_b32_e32 v20, v85, v20, vcc
	v_cmp_gt_u32_e32 vcc, v91, v55
	v_cmp_le_u32_e64 s[4:5], v91, v90
	s_and_b64 s[4:5], vcc, s[4:5]
	v_cmp_lt_i32_e32 vcc, s8, v91
	s_and_b64 vcc, s[4:5], vcc
	v_or_b32_e32 v91, v103, v66
	v_cndmask_b32_e32 v21, v85, v21, vcc
	v_cmp_gt_u32_e32 vcc, v91, v55
	v_cmp_le_u32_e64 s[4:5], v91, v90
	s_and_b64 s[4:5], vcc, s[4:5]
	v_cmp_lt_i32_e32 vcc, s8, v91
	s_and_b64 vcc, s[4:5], vcc
	v_cmp_lt_u32_e64 s[4:5], v91, v90
	v_cndmask_b32_e32 v14, v85, v14, vcc
	v_cmp_ge_u32_e32 vcc, v91, v55
	s_and_b64 s[4:5], vcc, s[4:5]
	v_cmp_le_i32_e32 vcc, s8, v91
	s_and_b64 vcc, s[4:5], vcc
	v_or_b32_e32 v92, 2, v91
	v_cndmask_b32_e32 v15, v85, v15, vcc
	v_cmp_gt_u32_e32 vcc, v92, v55
	v_cmp_le_u32_e64 s[4:5], v92, v90
	s_and_b64 s[4:5], vcc, s[4:5]
	v_cmp_lt_i32_e32 vcc, s8, v92
	s_and_b64 vcc, s[4:5], vcc
	v_or_b32_e32 v91, 3, v91
	v_cndmask_b32_e32 v16, v85, v16, vcc
	v_cmp_gt_u32_e32 vcc, v91, v55
	v_cmp_le_u32_e64 s[4:5], v91, v90
	s_and_b64 s[4:5], vcc, s[4:5]
	v_cmp_lt_i32_e32 vcc, s8, v91
	s_and_b64 vcc, s[4:5], vcc
	v_or_b32_e32 v91, v104, v66
	v_cndmask_b32_e32 v17, v85, v17, vcc
	v_cmp_gt_u32_e32 vcc, v91, v55
	v_cmp_le_u32_e64 s[4:5], v91, v90
	s_and_b64 s[4:5], vcc, s[4:5]
	v_cmp_lt_i32_e32 vcc, s8, v91
	s_and_b64 vcc, s[4:5], vcc
	v_cmp_lt_u32_e64 s[4:5], v91, v90
	v_cndmask_b32_e32 v10, v85, v10, vcc
	v_cmp_ge_u32_e32 vcc, v91, v55
	v_max3_f32 v89, v89, v34, v35
	s_and_b64 s[4:5], vcc, s[4:5]
	v_cmp_le_i32_e32 vcc, s8, v91
	v_max3_f32 v89, v89, v36, v37
	s_and_b64 vcc, s[4:5], vcc
	v_or_b32_e32 v92, 2, v91
	v_max3_f32 v89, v89, v30, v31
	v_cndmask_b32_e32 v11, v85, v11, vcc
	v_cmp_gt_u32_e32 vcc, v92, v55
	v_cmp_le_u32_e64 s[4:5], v92, v90
	v_max3_f32 v89, v89, v32, v33
	s_and_b64 s[4:5], vcc, s[4:5]
	v_cmp_lt_i32_e32 vcc, s8, v92
	v_max3_f32 v89, v89, v26, v27
	s_and_b64 vcc, s[4:5], vcc
	v_or_b32_e32 v91, 3, v91
	v_max3_f32 v89, v89, v28, v29
	v_cndmask_b32_e32 v12, v85, v12, vcc
	v_cmp_gt_u32_e32 vcc, v91, v55
	v_cmp_le_u32_e64 s[4:5], v91, v90
	v_max3_f32 v89, v89, v22, v23
	s_and_b64 s[4:5], vcc, s[4:5]
	v_cmp_lt_i32_e32 vcc, s8, v91
	v_max3_f32 v89, v89, v24, v25
	s_and_b64 vcc, s[4:5], vcc
	v_or_b32_e32 v91, v105, v66
	v_max3_f32 v89, v89, v18, v19
	v_cndmask_b32_e32 v13, v85, v13, vcc
	v_cmp_le_u32_e32 vcc, v91, v90
	v_max3_f32 v89, v89, v20, v21
	v_or_b32_e32 v92, 2, v91
	v_cndmask_b32_e32 v6, v85, v6, vcc
	v_cmp_lt_u32_e32 vcc, v91, v90
	v_max3_f32 v89, v89, v14, v15
	v_or_b32_e32 v91, 3, v91
	v_cndmask_b32_e32 v7, v85, v7, vcc
	v_cmp_le_u32_e32 vcc, v92, v90
	v_max3_f32 v89, v89, v16, v17
	v_max3_f32 v89, v89, v10, v11
	v_cndmask_b32_e32 v8, v85, v8, vcc
	v_cmp_le_u32_e32 vcc, v91, v90
	v_or_b32_e32 v91, v106, v66
	v_max3_f32 v89, v89, v12, v13
	v_cndmask_b32_e32 v9, v85, v9, vcc
	v_cmp_le_u32_e32 vcc, v91, v90
	v_or_b32_e32 v92, 2, v91
	v_max3_f32 v89, v89, v6, v7
	v_cndmask_b32_e32 v2, v85, v2, vcc
	v_cmp_lt_u32_e32 vcc, v91, v90
	v_or_b32_e32 v91, 3, v91
	v_max3_f32 v89, v89, v8, v9
	v_cndmask_b32_e32 v3, v85, v3, vcc
	v_cmp_le_u32_e32 vcc, v92, v90
	v_max3_f32 v89, v89, v2, v3
	v_add_u32_e32 v55, 16, v55
	v_cndmask_b32_e32 v4, v85, v4, vcc
	v_cmp_le_u32_e32 vcc, v91, v90
	s_nop 1
	v_cndmask_b32_e32 v5, v85, v5, vcc
	v_max3_f32 v89, v89, v4, v5
	ds_bpermute_b32 v90, v67, v89
	s_waitcnt lgkmcnt(0)
	v_max_f32_e32 v90, v90, v90
	v_max_f32_e32 v89, v89, v90
	ds_bpermute_b32 v90, v68, v89
	s_waitcnt lgkmcnt(0)
	v_max3_f32 v89, v89, v90, v53
	v_sub_f32_e32 v38, v38, v89
	v_mul_f32_e32 v38, 0x3fb8aa3b, v38
	v_sub_f32_e32 v39, v39, v89
	v_exp_f32_e32 v38, v38
	v_mul_f32_e32 v39, 0x3fb8aa3b, v39
	v_sub_f32_e32 v40, v40, v89
	v_exp_f32_e32 v39, v39
	v_mul_f32_e32 v40, 0x3fb8aa3b, v40
	v_sub_f32_e32 v41, v41, v89
	v_exp_f32_e32 v40, v40
	v_mul_f32_e32 v41, 0x3fb8aa3b, v41
	v_sub_f32_e32 v34, v34, v89
	v_exp_f32_e32 v41, v41
	v_mul_f32_e32 v34, 0x3fb8aa3b, v34
	v_sub_f32_e32 v35, v35, v89
	v_add_f32_e32 v90, 0, v38
	v_exp_f32_e32 v34, v34
	v_mul_f32_e32 v35, 0x3fb8aa3b, v35
	v_sub_f32_e32 v36, v36, v89
	v_add_f32_e32 v90, v39, v90
	v_exp_f32_e32 v35, v35
	v_mul_f32_e32 v36, 0x3fb8aa3b, v36
	v_sub_f32_e32 v37, v37, v89
	v_add_f32_e32 v90, v40, v90
	v_exp_f32_e32 v36, v36
	v_mul_f32_e32 v37, 0x3fb8aa3b, v37
	v_sub_f32_e32 v30, v30, v89
	v_add_f32_e32 v90, v41, v90
	v_exp_f32_e32 v37, v37
	v_mul_f32_e32 v30, 0x3fb8aa3b, v30
	v_sub_f32_e32 v31, v31, v89
	v_add_f32_e32 v90, v34, v90
	v_exp_f32_e32 v30, v30
	v_mul_f32_e32 v31, 0x3fb8aa3b, v31
	v_sub_f32_e32 v32, v32, v89
	v_add_f32_e32 v90, v35, v90
	v_exp_f32_e32 v31, v31
	v_mul_f32_e32 v32, 0x3fb8aa3b, v32
	v_sub_f32_e32 v33, v33, v89
	v_add_f32_e32 v90, v36, v90
	v_exp_f32_e32 v32, v32
	v_mul_f32_e32 v33, 0x3fb8aa3b, v33
	v_sub_f32_e32 v26, v26, v89
	v_add_f32_e32 v90, v37, v90
	v_exp_f32_e32 v33, v33
	v_mul_f32_e32 v26, 0x3fb8aa3b, v26
	v_sub_f32_e32 v27, v27, v89
	v_add_f32_e32 v90, v30, v90
	v_exp_f32_e32 v26, v26
	v_mul_f32_e32 v27, 0x3fb8aa3b, v27
	v_sub_f32_e32 v28, v28, v89
	v_add_f32_e32 v90, v31, v90
	v_exp_f32_e32 v27, v27
	v_mul_f32_e32 v28, 0x3fb8aa3b, v28
	v_sub_f32_e32 v29, v29, v89
	v_add_f32_e32 v90, v32, v90
	v_exp_f32_e32 v28, v28
	v_mul_f32_e32 v29, 0x3fb8aa3b, v29
	v_sub_f32_e32 v22, v22, v89
	v_add_f32_e32 v90, v33, v90
	v_exp_f32_e32 v29, v29
	v_mul_f32_e32 v22, 0x3fb8aa3b, v22
	v_add_f32_e32 v90, v26, v90
	v_exp_f32_e32 v91, v22
	v_add_f32_e32 v90, v27, v90
	v_add_f32_e32 v90, v28, v90
	v_sub_f32_e32 v23, v23, v89
	v_add_f32_e32 v90, v29, v90
	v_mul_f32_e32 v23, 0x3fb8aa3b, v23
	v_add_f32_e32 v22, v91, v90
	v_exp_f32_e32 v90, v23
	v_sub_f32_e32 v23, v24, v89
	v_mul_f32_e32 v23, 0x3fb8aa3b, v23
	v_exp_f32_e32 v92, v23
	v_sub_f32_e32 v23, v25, v89
	v_sub_f32_e32 v19, v19, v89
	v_mul_f32_e32 v23, 0x3fb8aa3b, v23
	v_sub_f32_e32 v18, v18, v89
	v_mul_f32_e32 v19, 0x3fb8aa3b, v19
	v_exp_f32_e32 v93, v23
	v_mul_f32_e32 v18, 0x3fb8aa3b, v18
	v_exp_f32_e32 v95, v19
	v_sub_f32_e32 v19, v20, v89
	v_exp_f32_e32 v94, v18
	v_mul_f32_e32 v19, 0x3fb8aa3b, v19
	v_add_f32_e32 v22, v90, v22
	v_exp_f32_e32 v96, v19
	v_sub_f32_e32 v19, v21, v89
	v_sub_f32_e32 v15, v15, v89
	v_add_f32_e32 v22, v92, v22
	v_mul_f32_e32 v19, 0x3fb8aa3b, v19
	v_sub_f32_e32 v14, v14, v89
	v_mul_f32_e32 v15, 0x3fb8aa3b, v15
	v_add_f32_e32 v22, v93, v22
	v_exp_f32_e32 v97, v19
	v_mul_f32_e32 v14, 0x3fb8aa3b, v14
	v_exp_f32_e32 v99, v15
	v_sub_f32_e32 v15, v16, v89
	v_add_f32_e32 v18, v94, v22
	v_exp_f32_e32 v98, v14
	v_mul_f32_e32 v15, 0x3fb8aa3b, v15
	v_add_f32_e32 v18, v95, v18
	v_exp_f32_e32 v100, v15
	v_sub_f32_e32 v15, v17, v89
	v_sub_f32_e32 v11, v11, v89
	v_add_f32_e32 v18, v96, v18
	v_mul_f32_e32 v15, 0x3fb8aa3b, v15
	v_sub_f32_e32 v10, v10, v89
	v_mul_f32_e32 v11, 0x3fb8aa3b, v11
	v_add_f32_e32 v18, v97, v18
	v_exp_f32_e32 v101, v15
	v_mul_f32_e32 v10, 0x3fb8aa3b, v10
	v_exp_f32_e32 v103, v11
	v_sub_f32_e32 v11, v12, v89
	v_add_f32_e32 v14, v98, v18
	v_exp_f32_e32 v102, v10
	v_mul_f32_e32 v11, 0x3fb8aa3b, v11
	v_add_f32_e32 v14, v99, v14
	v_exp_f32_e32 v104, v11
	v_sub_f32_e32 v11, v13, v89
	v_sub_f32_e32 v7, v7, v89
	v_add_f32_e32 v14, v100, v14
	v_mul_f32_e32 v11, 0x3fb8aa3b, v11
	v_sub_f32_e32 v6, v6, v89
	v_mul_f32_e32 v7, 0x3fb8aa3b, v7
	v_add_f32_e32 v14, v101, v14
	v_exp_f32_e32 v105, v11
	v_mul_f32_e32 v6, 0x3fb8aa3b, v6
	v_exp_f32_e32 v107, v7
	v_sub_f32_e32 v7, v8, v89
	v_add_f32_e32 v10, v102, v14
	v_exp_f32_e32 v106, v6
	v_mul_f32_e32 v7, 0x3fb8aa3b, v7
	v_add_f32_e32 v10, v103, v10
	v_exp_f32_e32 v108, v7
	v_sub_f32_e32 v7, v9, v89
	v_sub_f32_e32 v3, v3, v89
	v_add_f32_e32 v10, v104, v10
	v_mul_f32_e32 v7, 0x3fb8aa3b, v7
	v_sub_f32_e32 v2, v2, v89
	v_mul_f32_e32 v3, 0x3fb8aa3b, v3
	v_add_f32_e32 v10, v105, v10
	v_exp_f32_e32 v109, v7
	v_mul_f32_e32 v2, 0x3fb8aa3b, v2
	v_exp_f32_e32 v111, v3
	v_sub_f32_e32 v3, v4, v89
	v_add_f32_e32 v6, v106, v10
	v_exp_f32_e32 v110, v2
	v_mul_f32_e32 v3, 0x3fb8aa3b, v3
	v_add_f32_e32 v6, v107, v6
	v_exp_f32_e32 v112, v3
	v_sub_f32_e32 v3, v5, v89
	v_add_f32_e32 v6, v108, v6
	v_mul_f32_e32 v3, 0x3fb8aa3b, v3
	v_add_f32_e32 v6, v109, v6
	v_exp_f32_e32 v113, v3
	v_add_f32_e32 v2, v110, v6
	v_add_f32_e32 v2, v111, v2
	v_add_f32_e32 v2, v112, v2
	v_add_f32_e32 v2, v113, v2
	ds_bpermute_b32 v3, v67, v2
	s_nop 0
	s_nop 0
	s_nop 0
	s_waitcnt lgkmcnt(0)
	v_add_f32_e32 v2, v2, v3
	ds_bpermute_b32 v3, v68, v2
	s_waitcnt lgkmcnt(0)
	v_add_f32_e32 v2, v2, v3
	v_sub_f32_e32 v3, v53, v89
	v_mul_f32_e32 v3, 0x3fb8aa3b, v3
	v_exp_f32_e32 v3, v3
	s_nop 0
	v_add_f32_e32 v2, v3, v2
	v_div_scale_f32 v3, s[4:5], v2, v2, 1.0
	v_rcp_f32_e32 v4, v3
	s_nop 0
	v_fma_f32 v5, -v3, v4, 1.0
	v_fmac_f32_e32 v4, v5, v4
	v_div_scale_f32 v5, vcc, 1.0, v2, 1.0
	v_mul_f32_e32 v6, v5, v4
	v_fma_f32 v7, -v3, v6, v5
	v_fmac_f32_e32 v6, v7, v4
	v_fma_f32 v3, -v3, v6, v5
	v_div_fmas_f32 v3, v3, v4, v6
	v_div_fixup_f32 v89, v3, v2, 1.0
	v_mul_f32_e32 v2, v38, v89
	v_mul_f32_e32 v3, v39, v89
	v_cvt_pk_bf16_f32 v2, v2, v3
	v_mul_f32_e32 v3, v40, v89
	v_mul_f32_e32 v4, v41, v89
	v_cvt_pk_bf16_f32 v3, v3, v4
	v_mul_f32_e32 v4, v34, v89
	v_mul_f32_e32 v5, v35, v89
	v_cvt_pk_bf16_f32 v4, v4, v5
	v_mul_f32_e32 v5, v36, v89
	v_mul_f32_e32 v6, v37, v89
	v_cvt_pk_bf16_f32 v5, v5, v6
	s_nop 0
	s_nop 0
	s_nop 0
	s_nop 0
	s_nop 0
	s_nop 0
	s_waitcnt lgkmcnt(0)
	v_mfma_f32_16x16x32_bf16 v[6:9], v[194:197], v[2:5], 0
	v_mul_f32_e32 v22, v29, v89
	s_nop 0
	v_mfma_f32_16x16x32_bf16 v[10:13], v[198:201], v[2:5], 0
	s_nop 0
	v_mfma_f32_16x16x32_bf16 v[14:17], v[202:205], v[2:5], 0
	s_nop 0
	v_mfma_f32_16x16x32_bf16 v[2:5], v[206:209], v[2:5], 0
	v_mul_f32_e32 v18, v30, v89
	v_mul_f32_e32 v19, v31, v89
	v_cvt_pk_bf16_f32 v18, v18, v19
	v_mul_f32_e32 v19, v32, v89
	v_mul_f32_e32 v20, v33, v89
	v_cvt_pk_bf16_f32 v19, v19, v20
	v_mul_f32_e32 v20, v26, v89
	v_mul_f32_e32 v21, v27, v89
	v_cvt_pk_bf16_f32 v20, v20, v21
	v_mul_f32_e32 v21, v28, v89
	s_nop 0
	v_cvt_pk_bf16_f32 v21, v21, v22
	s_nop 0
	s_nop 0
	s_nop 0
	v_mfma_f32_16x16x32_bf16 v[6:9], v[210:213], v[18:21], v[6:9]
	s_nop 0
	s_nop 0
	s_nop 0
	v_mfma_f32_16x16x32_bf16 v[10:13], v[214:217], v[18:21], v[10:13]
	s_nop 0
	s_nop 0
	s_nop 0
	v_mfma_f32_16x16x32_bf16 v[14:17], v[218:221], v[18:21], v[14:17]
	s_nop 0
	s_nop 0
	s_nop 0
	s_nop 0
	v_mfma_f32_16x16x32_bf16 v[2:5], v[222:225], v[18:21], v[2:5]
	v_mul_f32_e32 v18, v91, v89
	v_mul_f32_e32 v19, v90, v89
	v_cvt_pk_bf16_f32 v18, v18, v19
	v_mul_f32_e32 v19, v92, v89
	v_mul_f32_e32 v20, v93, v89
	v_cvt_pk_bf16_f32 v19, v19, v20
	v_mul_f32_e32 v20, v94, v89
	v_mul_f32_e32 v21, v95, v89
	v_cvt_pk_bf16_f32 v20, v20, v21
	v_mul_f32_e32 v21, v96, v89
	v_mul_f32_e32 v22, v97, v89
	v_cvt_pk_bf16_f32 v21, v21, v22
	s_nop 0
	s_nop 0
	s_nop 0
	v_mfma_f32_16x16x32_bf16 v[6:9], v[226:229], v[18:21], v[6:9]
	s_nop 0
	s_nop 0
	s_nop 0
	v_mfma_f32_16x16x32_bf16 v[10:13], v[230:233], v[18:21], v[10:13]
	s_nop 0
	s_nop 0
	s_nop 0
	v_mfma_f32_16x16x32_bf16 v[14:17], v[234:237], v[18:21], v[14:17]
	s_nop 0
	s_nop 0
	s_nop 0
	s_nop 0
	v_mfma_f32_16x16x32_bf16 v[2:5], v[238:241], v[18:21], v[2:5]
	v_mul_f32_e32 v18, v98, v89
	v_mul_f32_e32 v19, v99, v89
	v_cvt_pk_bf16_f32 v18, v18, v19
	v_mul_f32_e32 v19, v100, v89
	v_mul_f32_e32 v20, v101, v89
	v_cvt_pk_bf16_f32 v19, v19, v20
	v_mul_f32_e32 v20, v102, v89
	v_mul_f32_e32 v21, v103, v89
	v_cvt_pk_bf16_f32 v20, v20, v21
	v_mul_f32_e32 v21, v104, v89
	v_mul_f32_e32 v22, v105, v89
	v_cvt_pk_bf16_f32 v21, v21, v22
	s_nop 0
	s_nop 0
	s_nop 0
	v_mfma_f32_16x16x32_bf16 v[6:9], v[114:117], v[18:21], v[6:9]
	s_nop 0
	s_nop 0
	s_nop 0
	v_mfma_f32_16x16x32_bf16 v[10:13], v[118:121], v[18:21], v[10:13]
	s_nop 0
	s_nop 0
	s_nop 0
	v_mfma_f32_16x16x32_bf16 v[14:17], v[122:125], v[18:21], v[14:17]
	s_nop 0
	s_nop 0
	s_nop 0
	s_nop 0
	v_mfma_f32_16x16x32_bf16 v[18:21], v[126:129], v[18:21], v[2:5]
	s_nop 2
	v_mul_f32_e32 v2, v106, v89
	v_mul_f32_e32 v3, v107, v89
	v_cvt_pk_bf16_f32 v22, v2, v3
	v_mul_f32_e32 v2, v108, v89
	v_mul_f32_e32 v3, v109, v89
	v_cvt_pk_bf16_f32 v23, v2, v3
	v_mul_f32_e32 v2, v110, v89
	v_mul_f32_e32 v3, v111, v89
	v_cvt_pk_bf16_f32 v24, v2, v3
	v_mul_f32_e32 v2, v112, v89
	v_mul_f32_e32 v3, v113, v89
	v_cvt_pk_bf16_f32 v25, v2, v3
	s_nop 0
	s_nop 0
	s_nop 0
	v_mfma_f32_16x16x32_bf16 v[2:5], v[130:133], v[22:25], v[6:9]
	s_nop 2
	s_nop 0
	s_nop 0
	s_nop 2
	v_cvt_pk_bf16_f32 v2, v2, v3
	s_nop 0
	v_mfma_f32_16x16x32_bf16 v[6:9], v[134:137], v[22:25], v[10:13]
	s_nop 2
	s_nop 0
	s_nop 0
	v_cvt_pk_bf16_f32 v3, v4, v5
	s_nop 0
	v_mfma_f32_16x16x32_bf16 v[10:13], v[138:141], v[22:25], v[14:17]
	s_nop 2
	s_nop 0
	s_nop 0
	s_nop 0
	v_mfma_f32_16x16x32_bf16 v[14:17], v[142:145], v[22:25], v[18:21]
	s_nop 2
	v_lshl_add_u64 v[18:19], v[62:63], 0, s[10:11]
	global_store_dwordx2 v[18:19], v[2:3], off offset:-64
	v_cvt_pk_bf16_f32 v2, v6, v7
	v_cvt_pk_bf16_f32 v3, v8, v9
	s_add_u32 s10, s10, 0x8000
	global_store_dwordx2 v[18:19], v[2:3], off offset:-32
	v_cvt_pk_bf16_f32 v2, v10, v11
	v_cvt_pk_bf16_f32 v3, v12, v13
	s_addc_u32 s11, s11, 0
	global_store_dwordx2 v[18:19], v[2:3], off
	v_cvt_pk_bf16_f32 v2, v14, v15
	v_cvt_pk_bf16_f32 v3, v16, v17
	s_cmp_eq_u32 s10, 0x20000
	global_store_dwordx2 v[18:19], v[2:3], off offset:32
	s_cbranch_scc0 .LBB0_559
	s_add_i32 s14, s14, s3
	s_add_i32 s18, s18, s19
	s_cmpk_gt_i32 s14, 0x1ff
	s_cbranch_scc0 .LBB0_549

	.amdhsa_kernel _Z4mega4Args
		.amdhsa_group_segment_fixed_size 0
		.amdhsa_private_segment_fixed_size 0
		.amdhsa_kernarg_size 472
		.amdhsa_user_sgpr_count 2
		.amdhsa_user_sgpr_dispatch_ptr 0
		.amdhsa_user_sgpr_queue_ptr 0
		.amdhsa_user_sgpr_kernarg_segment_ptr 1
		.amdhsa_user_sgpr_dispatch_id 0
		.amdhsa_user_sgpr_kernarg_preload_length 0
		.amdhsa_user_sgpr_kernarg_preload_offset 0
		.amdhsa_user_sgpr_private_segment_size 0
		.amdhsa_uses_dynamic_stack 0
		.amdhsa_enable_private_segment 0
		.amdhsa_system_sgpr_workgroup_id_x 1
		.amdhsa_system_sgpr_workgroup_id_y 0
		.amdhsa_system_sgpr_workgroup_id_z 0
		.amdhsa_system_sgpr_workgroup_info 0
		.amdhsa_system_vgpr_workitem_id 0
		.amdhsa_next_free_vgpr 256
		.amdhsa_next_free_sgpr 98
		.amdhsa_accum_offset 256
		.amdhsa_reserve_vcc 1
		.amdhsa_float_round_mode_32 0
		.amdhsa_float_round_mode_16_64 0
		.amdhsa_float_denorm_mode_32 3
		.amdhsa_float_denorm_mode_16_64 3
		.amdhsa_dx10_clamp 1
		.amdhsa_ieee_mode 1
		.amdhsa_fp16_overflow 0
		.amdhsa_tg_split 0
		.amdhsa_exception_fp_ieee_invalid_op 0
		.amdhsa_exception_fp_denorm_src 0
		.amdhsa_exception_fp_ieee_div_zero 0
		.amdhsa_exception_fp_ieee_overflow 0
		.amdhsa_exception_fp_ieee_underflow 0
		.amdhsa_exception_fp_ieee_inexact 0
		.amdhsa_exception_int_div_zero 0
	.end_amdhsa_kernel

amdhsa.kernels:
  - .agpr_count:     0
    .args:
      - .offset:         0
        .size:           216
        .value_kind:     by_value
      - .offset:         216
        .size:           4
        .value_kind:     hidden_block_count_x
      - .offset:         220
        .size:           4
        .value_kind:     hidden_block_count_y
      - .offset:         224
        .size:           4
        .value_kind:     hidden_block_count_z
      - .offset:         228
        .size:           2
        .value_kind:     hidden_group_size_x
      - .offset:         230
        .size:           2
        .value_kind:     hidden_group_size_y
      - .offset:         232
        .size:           2
        .value_kind:     hidden_group_size_z
      - .offset:         234
        .size:           2
        .value_kind:     hidden_remainder_x
      - .offset:         236
        .size:           2
        .value_kind:     hidden_remainder_y
      - .offset:         238
        .size:           2
        .value_kind:     hidden_remainder_z
      - .offset:         256
        .size:           8
        .value_kind:     hidden_global_offset_x
      - .offset:         264
        .size:           8
        .value_kind:     hidden_global_offset_y
      - .offset:         272
        .size:           8
        .value_kind:     hidden_global_offset_z
      - .offset:         280
        .size:           2
        .value_kind:     hidden_grid_dims
      - .offset:         336
        .size:           4
        .value_kind:     hidden_dynamic_lds_size
    .group_segment_fixed_size: 0
    .kernarg_segment_align: 8
    .kernarg_segment_size: 472
    .language:       OpenCL C
    .language_version:
      - 2
      - 0
    .max_flat_workgroup_size: 512
    .name:           _Z4mega4Args
    .private_segment_fixed_size: 0
    .sgpr_count:     104
    .sgpr_spill_count: 2
    .symbol:         _Z4mega4Args.kd
    .uniform_work_group_size: 1
    .uses_dynamic_stack: false
    .vgpr_count:     256
    .vgpr_spill_count: 0
    .wavefront_size: 64
